# speedup vs baseline: 1.0151x; 1.0151x over previous
_Z11edge_kernelILi36ELb1EEvPKfS1_PKDF16_PKiS5_S1_S1_S1_S1_S1_PDF16_:
	s_load_dwordx8 s[4:11], s[0:1], 0x0
	s_load_dwordx8 s[12:19], s[0:1], 0x20
	s_load_dwordx4 s[20:23], s[0:1], 0x40
	s_load_dwordx2 s[24:25], s[0:1], 0x50
	v_readfirstlane_b32 s3, v0
	v_bfe_u32 v75, v0, 4, 2
	v_and_b32_e32 v76, 15, v0
	v_and_b32_e32 v78, 63, v0
	s_lshr_b32 s3, s3, 6
	s_lshl_b32 s2, s2, 1
	s_add_i32 s2, s2, s3
	v_lshlrev_b32_e32 v74, 8, v75
	v_lshl_or_b32 v74, v76, 4, v74
	v_lshlrev_b32_e32 v79, 4, v78
	v_lshl_or_b32 v77, v76, 2, v75
	v_lshlrev_b32_e32 v77, 2, v77
	v_mul_u32_u24_e32 v73, 0x900, v75
	v_lshl_or_b32 v73, v76, 4, v73
	v_mul_u32_u24_e32 v78, 36, v75
	s_mul_i32 s28, s2, 0x2400
	s_lshl_b32 s29, s2, 14
	s_lshl_b32 s30, s2, 2
	s_lshl_b32 s31, s2, 8
	s_lshl_b32 s33, s3, 10
	s_lshl_b32 s34, s3, 8
	s_addk_i32 s34, 0x4000
	s_waitcnt lgkmcnt(0)
	s_add_u32 s10, s10, s30
	s_addc_u32 s11, s11, 0
	s_add_u32 s12, s12, s30
	s_addc_u32 s13, s13, 0
	s_load_dword s35, s[10:11], 0x0
	s_load_dword s36, s[12:13], 0x0
	s_add_u32 s14, s14, s28
	s_addc_u32 s15, s15, 0
	global_load_dwordx4 v[0:3], v73, s[14:15] nt
	global_load_dwordx4 v[4:7], v73, s[14:15] offset:256 nt
	global_load_dwordx4 v[8:11], v73, s[14:15] offset:512 nt
	global_load_dwordx4 v[12:15], v73, s[14:15] offset:768 nt
	global_load_dwordx4 v[16:19], v73, s[14:15] offset:1024 nt
	global_load_dwordx4 v[20:23], v73, s[14:15] offset:1280 nt
	global_load_dwordx4 v[24:27], v73, s[14:15] offset:1536 nt
	global_load_dwordx4 v[28:31], v73, s[14:15] offset:1792 nt
	global_load_dwordx4 v[32:35], v73, s[14:15] offset:2048 nt
	s_add_u32 s22, s22, s33
	s_addc_u32 s23, s23, 0
	s_add_u32 s18, s18, s29
	s_addc_u32 s19, s19, 0
	s_mov_b32 m0, s33
	s_nop 0
	global_load_lds_dwordx4 v79, s[22:23]
	global_load_lds_dwordx4 v79, s[22:23] offset:2048
	s_add_u32 m0, m0, 0x1000
	s_add_u32 s22, s22, 0x1000
	s_addc_u32 s23, s23, 0
	global_load_lds_dwordx4 v79, s[22:23]
	global_load_lds_dwordx4 v79, s[22:23] offset:2048
	s_add_u32 m0, m0, 0x1000
	s_add_u32 s22, s22, 0x1000
	s_addc_u32 s23, s23, 0
	global_load_lds_dwordx4 v79, s[22:23]
	global_load_lds_dwordx4 v79, s[22:23] offset:2048
	s_add_u32 m0, m0, 0x1000
	s_add_u32 s22, s22, 0x1000
	s_addc_u32 s23, s23, 0
	global_load_lds_dwordx4 v79, s[22:23]
	global_load_lds_dwordx4 v79, s[22:23] offset:2048
	s_add_u32 s16, s16, s31
	s_addc_u32 s17, s17, 0
	s_add_u32 s20, s20, s31
	s_addc_u32 s21, s21, 0
	s_waitcnt lgkmcnt(0)
	s_lshl_b32 s36, s36, 7
	s_add_u32 s24, s24, s36
	s_addc_u32 s25, s25, 0
	s_lshl_b32 s37, s35, 7
	s_lshl_b32 s38, s35, 4
	s_add_u32 s4, s4, s37
	s_addc_u32 s5, s5, 0
	s_add_u32 s6, s6, s38
	s_addc_u32 s7, s7, 0
	v_mov_b32_e32 v93, 0
	v_mov_b32_e32 v92, v78
	v_lshl_add_u64 v[94:95], s[4:5], 0, v[92:93]
	v_lshl_add_u64 v[94:95], v[94:95], 0, 20
	v_cmp_eq_u32_e32 vcc, 3, v75
	s_nop 1
	v_mov_b32_e32 v90, s6
	v_mov_b32_e32 v91, s7
	v_cndmask_b32_e32 v94, v94, v90, vcc
	v_cndmask_b32_e32 v95, v95, v91, vcc
	global_load_dwordx4 v[80:83], v78, s[4:5] nt
	global_load_dword v84, v78, s[4:5] offset:16 nt
	global_load_dwordx4 v[86:89], v[94:95], off nt
	global_load_dword v72, v77, s[16:17] nt
	global_load_dword v64, v77, s[20:21] nt
	v_add_u32_e32 v78, s34, v77
	v_lshl_add_u32 v79, v75, 2, s34
	s_waitcnt vmcnt(2)
	s_barrier
	s_setprio 3
	v_pk_mul_f32 v[96:97], v[80:81], v[0:1] op_sel_hi:[0,1]
	v_pk_mul_f32 v[98:99], v[80:81], v[2:3] op_sel_hi:[0,1]
	v_pk_mul_f32 v[100:101], v[80:81], v[4:5] op_sel:[1,0]
	v_pk_mul_f32 v[102:103], v[80:81], v[6:7] op_sel:[1,0]
	v_pk_fma_f32 v[96:97], v[82:83], v[8:9], v[96:97] op_sel_hi:[0,1,1]
	v_pk_fma_f32 v[98:99], v[82:83], v[10:11], v[98:99] op_sel_hi:[0,1,1]
	v_pk_fma_f32 v[100:101], v[82:83], v[12:13], v[100:101] op_sel:[1,0,0]
	v_pk_fma_f32 v[102:103], v[82:83], v[14:15], v[102:103] op_sel:[1,0,0]
	v_pk_fma_f32 v[96:97], v[84:85], v[16:17], v[96:97] op_sel_hi:[0,1,1]
	v_pk_fma_f32 v[98:99], v[84:85], v[18:19], v[98:99] op_sel_hi:[0,1,1]
	v_pk_fma_f32 v[100:101], v[86:87], v[20:21], v[100:101] op_sel_hi:[0,1,1]
	v_pk_fma_f32 v[102:103], v[86:87], v[22:23], v[102:103] op_sel_hi:[0,1,1]
	v_pk_fma_f32 v[96:97], v[86:87], v[24:25], v[96:97] op_sel:[1,0,0]
	v_pk_fma_f32 v[98:99], v[86:87], v[26:27], v[98:99] op_sel:[1,0,0]
	v_pk_fma_f32 v[100:101], v[88:89], v[28:29], v[100:101] op_sel_hi:[0,1,1]
	v_pk_fma_f32 v[102:103], v[88:89], v[30:31], v[102:103] op_sel_hi:[0,1,1]
	v_pk_fma_f32 v[96:97], v[88:89], v[32:33], v[96:97] op_sel:[1,0,0]
	v_pk_fma_f32 v[98:99], v[88:89], v[34:35], v[98:99] op_sel:[1,0,0]
	v_pk_add_f32 v[96:97], v[96:97], v[100:101]
	v_pk_add_f32 v[98:99], v[98:99], v[102:103]
	s_nop 1
	v_permlane16_swap_b32_e32 v96, v97
	v_permlane16_swap_b32_e32 v98, v99
	v_add_f32_e32 v96, v96, v97
	v_add_f32_e32 v98, v98, v99
	s_nop 1
	v_permlane32_swap_b32_e32 v96, v98
	v_add_f32_e32 v96, v96, v98
	s_waitcnt vmcnt(1)
	v_add_f32_e32 v96, v96, v72
	v_max_f32_e32 v96, 0, v96
	ds_write_b32 v78, v96
	ds_read2_b32 v[80:81], v79 offset0:0 offset1:4
	ds_read2_b32 v[82:83], v79 offset0:8 offset1:12
	ds_read2_b32 v[84:85], v79 offset0:16 offset1:20
	ds_read2_b32 v[86:87], v79 offset0:24 offset1:28
	ds_read2_b32 v[88:89], v79 offset0:32 offset1:36
	ds_read2_b32 v[90:91], v79 offset0:40 offset1:44
	ds_read2_b32 v[92:93], v79 offset0:48 offset1:52
	ds_read2_b32 v[94:95], v79 offset0:56 offset1:60
	s_waitcnt lgkmcnt(0)
	v_cmp_neq_f32_e64 s[40:41], 0, v80
	v_cmp_neq_f32_e64 s[42:43], 0, v81
	v_cmp_neq_f32_e64 s[44:45], 0, v82
	v_cmp_neq_f32_e64 s[46:47], 0, v83
	v_cmp_neq_f32_e64 s[48:49], 0, v84
	v_cmp_neq_f32_e64 s[50:51], 0, v85
	v_cmp_neq_f32_e64 s[52:53], 0, v86
	v_cmp_neq_f32_e64 s[54:55], 0, v87
	v_cmp_neq_f32_e64 s[56:57], 0, v88
	v_cmp_neq_f32_e64 s[58:59], 0, v89
	v_cmp_neq_f32_e64 s[60:61], 0, v90
	v_cmp_neq_f32_e64 s[62:63], 0, v91
	v_cmp_neq_f32_e64 s[64:65], 0, v92
	v_cmp_neq_f32_e64 s[66:67], 0, v93
	v_cmp_neq_f32_e64 s[68:69], 0, v94
	v_cmp_neq_f32_e64 s[70:71], 0, v95
	s_mov_b64 exec, s[40:41]
	global_load_dwordx4 v[0:3], v74, s[18:19] nt
	s_mov_b64 exec, s[42:43]
	global_load_dwordx4 v[4:7], v74, s[18:19] offset:1024 nt
	s_mov_b64 exec, s[44:45]
	global_load_dwordx4 v[8:11], v74, s[18:19] offset:2048 nt
	s_mov_b64 exec, s[46:47]
	global_load_dwordx4 v[12:15], v74, s[18:19] offset:3072 nt
	s_add_u32 s18, s18, 0x1000
	s_addc_u32 s19, s19, 0
	s_mov_b64 exec, s[48:49]
	global_load_dwordx4 v[16:19], v74, s[18:19] nt
	s_mov_b64 exec, s[50:51]
	global_load_dwordx4 v[20:23], v74, s[18:19] offset:1024 nt
	s_mov_b64 exec, s[52:53]
	global_load_dwordx4 v[24:27], v74, s[18:19] offset:2048 nt
	s_mov_b64 exec, s[54:55]
	global_load_dwordx4 v[28:31], v74, s[18:19] offset:3072 nt
	s_add_u32 s18, s18, 0x1000
	s_addc_u32 s19, s19, 0
	s_mov_b64 exec, s[56:57]
	global_load_dwordx4 v[32:35], v74, s[18:19] nt
	s_mov_b64 exec, s[58:59]
	global_load_dwordx4 v[36:39], v74, s[18:19] offset:1024 nt
	s_mov_b64 exec, s[60:61]
	global_load_dwordx4 v[40:43], v74, s[18:19] offset:2048 nt
	s_mov_b64 exec, s[62:63]
	global_load_dwordx4 v[44:47], v74, s[18:19] offset:3072 nt
	s_add_u32 s18, s18, 0x1000
	s_addc_u32 s19, s19, 0
	s_mov_b64 exec, s[64:65]
	global_load_dwordx4 v[48:51], v74, s[18:19] nt
	s_mov_b64 exec, s[66:67]
	global_load_dwordx4 v[52:55], v74, s[18:19] offset:1024 nt
	s_mov_b64 exec, s[68:69]
	global_load_dwordx4 v[56:59], v74, s[18:19] offset:2048 nt
	s_mov_b64 exec, s[70:71]
	global_load_dwordx4 v[60:63], v74, s[18:19] offset:3072 nt
	s_mov_b64 exec, -1
	v_mov_b32_e32 v96, 0
	v_mov_b32_e32 v97, 0
	v_mov_b32_e32 v98, 0
	v_mov_b32_e32 v99, 0
	v_mov_b32_e32 v100, 0
	v_mov_b32_e32 v101, 0
	v_mov_b32_e32 v102, 0
	v_mov_b32_e32 v103, 0
	s_waitcnt vmcnt(0)
	s_mov_b64 exec, s[40:41]
	v_pk_fma_f32 v[96:97], v[80:81], v[0:1], v[96:97] op_sel_hi:[0,1,1]
	v_pk_fma_f32 v[98:99], v[80:81], v[2:3], v[98:99] op_sel_hi:[0,1,1]
	s_mov_b64 exec, s[42:43]
	v_pk_fma_f32 v[100:101], v[80:81], v[4:5], v[100:101] op_sel:[1,0,0]
	v_pk_fma_f32 v[102:103], v[80:81], v[6:7], v[102:103] op_sel:[1,0,0]
	s_mov_b64 exec, s[44:45]
	v_pk_fma_f32 v[96:97], v[82:83], v[8:9], v[96:97] op_sel_hi:[0,1,1]
	v_pk_fma_f32 v[98:99], v[82:83], v[10:11], v[98:99] op_sel_hi:[0,1,1]
	s_mov_b64 exec, s[46:47]
	v_pk_fma_f32 v[100:101], v[82:83], v[12:13], v[100:101] op_sel:[1,0,0]
	v_pk_fma_f32 v[102:103], v[82:83], v[14:15], v[102:103] op_sel:[1,0,0]
	s_mov_b64 exec, s[48:49]
	v_pk_fma_f32 v[96:97], v[84:85], v[16:17], v[96:97] op_sel_hi:[0,1,1]
	v_pk_fma_f32 v[98:99], v[84:85], v[18:19], v[98:99] op_sel_hi:[0,1,1]
	s_mov_b64 exec, s[50:51]
	v_pk_fma_f32 v[100:101], v[84:85], v[20:21], v[100:101] op_sel:[1,0,0]
	v_pk_fma_f32 v[102:103], v[84:85], v[22:23], v[102:103] op_sel:[1,0,0]
	s_mov_b64 exec, s[52:53]
	v_pk_fma_f32 v[96:97], v[86:87], v[24:25], v[96:97] op_sel_hi:[0,1,1]
	v_pk_fma_f32 v[98:99], v[86:87], v[26:27], v[98:99] op_sel_hi:[0,1,1]
	s_mov_b64 exec, s[54:55]
	v_pk_fma_f32 v[100:101], v[86:87], v[28:29], v[100:101] op_sel:[1,0,0]
	v_pk_fma_f32 v[102:103], v[86:87], v[30:31], v[102:103] op_sel:[1,0,0]
	s_mov_b64 exec, s[56:57]
	v_pk_fma_f32 v[96:97], v[88:89], v[32:33], v[96:97] op_sel_hi:[0,1,1]
	v_pk_fma_f32 v[98:99], v[88:89], v[34:35], v[98:99] op_sel_hi:[0,1,1]
	s_mov_b64 exec, s[58:59]
	v_pk_fma_f32 v[100:101], v[88:89], v[36:37], v[100:101] op_sel:[1,0,0]
	v_pk_fma_f32 v[102:103], v[88:89], v[38:39], v[102:103] op_sel:[1,0,0]
	s_mov_b64 exec, s[60:61]
	v_pk_fma_f32 v[96:97], v[90:91], v[40:41], v[96:97] op_sel_hi:[0,1,1]
	v_pk_fma_f32 v[98:99], v[90:91], v[42:43], v[98:99] op_sel_hi:[0,1,1]
	s_mov_b64 exec, s[62:63]
	v_pk_fma_f32 v[100:101], v[90:91], v[44:45], v[100:101] op_sel:[1,0,0]
	v_pk_fma_f32 v[102:103], v[90:91], v[46:47], v[102:103] op_sel:[1,0,0]
	s_mov_b64 exec, s[64:65]
	v_pk_fma_f32 v[96:97], v[92:93], v[48:49], v[96:97] op_sel_hi:[0,1,1]
	v_pk_fma_f32 v[98:99], v[92:93], v[50:51], v[98:99] op_sel_hi:[0,1,1]
	s_mov_b64 exec, s[66:67]
	v_pk_fma_f32 v[100:101], v[92:93], v[52:53], v[100:101] op_sel:[1,0,0]
	v_pk_fma_f32 v[102:103], v[92:93], v[54:55], v[102:103] op_sel:[1,0,0]
	s_mov_b64 exec, s[68:69]
	v_pk_fma_f32 v[96:97], v[94:95], v[56:57], v[96:97] op_sel_hi:[0,1,1]
	v_pk_fma_f32 v[98:99], v[94:95], v[58:59], v[98:99] op_sel_hi:[0,1,1]
	s_mov_b64 exec, s[70:71]
	v_pk_fma_f32 v[100:101], v[94:95], v[60:61], v[100:101] op_sel:[1,0,0]
	v_pk_fma_f32 v[102:103], v[94:95], v[62:63], v[102:103] op_sel:[1,0,0]
	s_mov_b64 exec, -1
	ds_read_b128 v[0:3], v74
	ds_read_b128 v[4:7], v74 offset:1024
	ds_read_b128 v[8:11], v74 offset:2048
	ds_read_b128 v[12:15], v74 offset:3072
	ds_read_b128 v[16:19], v74 offset:4096
	ds_read_b128 v[20:23], v74 offset:5120
	ds_read_b128 v[24:27], v74 offset:6144
	ds_read_b128 v[28:31], v74 offset:7168
	ds_read_b128 v[32:35], v74 offset:8192
	ds_read_b128 v[36:39], v74 offset:9216
	ds_read_b128 v[40:43], v74 offset:10240
	ds_read_b128 v[44:47], v74 offset:11264
	ds_read_b128 v[48:51], v74 offset:12288
	ds_read_b128 v[52:55], v74 offset:13312
	ds_read_b128 v[56:59], v74 offset:14336
	v_pk_add_f32 v[96:97], v[96:97], v[100:101]
	v_pk_add_f32 v[98:99], v[98:99], v[102:103]
	s_nop 1
	v_permlane16_swap_b32_e32 v96, v97
	v_permlane16_swap_b32_e32 v98, v99
	v_add_f32_e32 v96, v96, v97
	v_add_f32_e32 v98, v98, v99
	s_nop 1
	v_permlane32_swap_b32_e32 v96, v98
	v_add_f32_e32 v96, v96, v98
	v_add_f32_e32 v96, v96, v64
	s_waitcnt lgkmcnt(5)
	ds_read_b128 v[60:63], v74 offset:15360
	ds_write_b32 v78, v96
	ds_read2_b32 v[80:81], v79 offset0:0 offset1:4
	ds_read2_b32 v[82:83], v79 offset0:8 offset1:12
	ds_read2_b32 v[84:85], v79 offset0:16 offset1:20
	ds_read2_b32 v[86:87], v79 offset0:24 offset1:28
	ds_read2_b32 v[88:89], v79 offset0:32 offset1:36
	ds_read2_b32 v[90:91], v79 offset0:40 offset1:44
	ds_read2_b32 v[92:93], v79 offset0:48 offset1:52
	ds_read2_b32 v[94:95], v79 offset0:56 offset1:60
	v_lshlrev_b32_e32 v72, 3, v76
	v_lshl_or_b32 v72, v75, 2, v72
	v_cmp_gt_u32_e32 vcc, 2, v75
	s_waitcnt lgkmcnt(0)
	v_pk_mul_f32 v[96:97], v[80:81], v[0:1] op_sel_hi:[0,1]
	v_pk_mul_f32 v[98:99], v[80:81], v[2:3] op_sel_hi:[0,1]
	v_pk_mul_f32 v[100:101], v[80:81], v[4:5] op_sel:[1,0]
	v_pk_mul_f32 v[102:103], v[80:81], v[6:7] op_sel:[1,0]
	v_pk_fma_f32 v[96:97], v[82:83], v[8:9], v[96:97] op_sel_hi:[0,1,1]
	v_pk_fma_f32 v[98:99], v[82:83], v[10:11], v[98:99] op_sel_hi:[0,1,1]
	v_pk_fma_f32 v[100:101], v[82:83], v[12:13], v[100:101] op_sel:[1,0,0]
	v_pk_fma_f32 v[102:103], v[82:83], v[14:15], v[102:103] op_sel:[1,0,0]
	v_pk_fma_f32 v[96:97], v[84:85], v[16:17], v[96:97] op_sel_hi:[0,1,1]
	v_pk_fma_f32 v[98:99], v[84:85], v[18:19], v[98:99] op_sel_hi:[0,1,1]
	v_pk_fma_f32 v[100:101], v[84:85], v[20:21], v[100:101] op_sel:[1,0,0]
	v_pk_fma_f32 v[102:103], v[84:85], v[22:23], v[102:103] op_sel:[1,0,0]
	v_pk_fma_f32 v[96:97], v[86:87], v[24:25], v[96:97] op_sel_hi:[0,1,1]
	v_pk_fma_f32 v[98:99], v[86:87], v[26:27], v[98:99] op_sel_hi:[0,1,1]
	v_pk_fma_f32 v[100:101], v[86:87], v[28:29], v[100:101] op_sel:[1,0,0]
	v_pk_fma_f32 v[102:103], v[86:87], v[30:31], v[102:103] op_sel:[1,0,0]
	v_pk_fma_f32 v[96:97], v[88:89], v[32:33], v[96:97] op_sel_hi:[0,1,1]
	v_pk_fma_f32 v[98:99], v[88:89], v[34:35], v[98:99] op_sel_hi:[0,1,1]
	v_pk_fma_f32 v[100:101], v[88:89], v[36:37], v[100:101] op_sel:[1,0,0]
	v_pk_fma_f32 v[102:103], v[88:89], v[38:39], v[102:103] op_sel:[1,0,0]
	v_pk_fma_f32 v[96:97], v[90:91], v[40:41], v[96:97] op_sel_hi:[0,1,1]
	v_pk_fma_f32 v[98:99], v[90:91], v[42:43], v[98:99] op_sel_hi:[0,1,1]
	v_pk_fma_f32 v[100:101], v[90:91], v[44:45], v[100:101] op_sel:[1,0,0]
	v_pk_fma_f32 v[102:103], v[90:91], v[46:47], v[102:103] op_sel:[1,0,0]
	v_pk_fma_f32 v[96:97], v[92:93], v[48:49], v[96:97] op_sel_hi:[0,1,1]
	v_pk_fma_f32 v[98:99], v[92:93], v[50:51], v[98:99] op_sel_hi:[0,1,1]
	v_pk_fma_f32 v[100:101], v[92:93], v[52:53], v[100:101] op_sel:[1,0,0]
	v_pk_fma_f32 v[102:103], v[92:93], v[54:55], v[102:103] op_sel:[1,0,0]
	v_pk_fma_f32 v[96:97], v[94:95], v[56:57], v[96:97] op_sel_hi:[0,1,1]
	v_pk_fma_f32 v[98:99], v[94:95], v[58:59], v[98:99] op_sel_hi:[0,1,1]
	v_pk_fma_f32 v[100:101], v[94:95], v[60:61], v[100:101] op_sel:[1,0,0]
	v_pk_fma_f32 v[102:103], v[94:95], v[62:63], v[102:103] op_sel:[1,0,0]
	v_pk_add_f32 v[96:97], v[96:97], v[100:101]
	v_pk_add_f32 v[98:99], v[98:99], v[102:103]
	s_nop 1
	v_permlane16_swap_b32_e32 v96, v98
	v_permlane16_swap_b32_e32 v97, v99
	v_add_f32_e32 v96, v96, v98
	v_add_f32_e32 v97, v97, v99
	v_mov_b32_e32 v80, v96
	v_mov_b32_e32 v81, v97
	s_nop 1
	v_permlane32_swap_b32_e32 v96, v80
	v_permlane32_swap_b32_e32 v97, v81
	v_add_f32_e32 v96, v96, v80
	v_add_f32_e32 v97, v97, v81
	v_cvt_pk_f16_f32 v73, v96, v97
	s_and_saveexec_b64 s[4:5], vcc
	global_atomic_pk_add_f16 v72, v73, s[24:25]
	s_endpgm
	.p2align	8

_Z11edge_kernelILi64ELb0EEvPKfS1_PKDF16_PKiS5_S1_S1_S1_S1_S1_PDF16_:
	s_load_dwordx16 s[4:19], s[0:1], 0x10
	s_load_dwordx2 s[20:21], s[0:1], 0x50
	v_readfirstlane_b32 s3, v0
	v_bfe_u32 v75, v0, 4, 2
	v_and_b32_e32 v76, 15, v0
	v_and_b32_e32 v78, 63, v0
	s_lshr_b32 s3, s3, 6
	s_lshl_b32 s2, s2, 1
	s_add_i32 s2, s2, s3
	v_lshlrev_b32_e32 v74, 8, v75
	v_lshl_or_b32 v74, v76, 4, v74
	v_lshlrev_b32_e32 v79, 4, v78
	v_lshl_or_b32 v77, v76, 2, v75
	v_lshlrev_b32_e32 v77, 2, v77
	v_lshlrev_b32_e32 v78, 5, v75
	v_lshlrev_b32_e32 v73, 12, v75
	v_lshl_or_b32 v73, v76, 4, v73
	s_lshl_b32 s28, s2, 14
	s_lshl_b32 s29, s2, 14
	s_lshl_b32 s30, s2, 2
	s_lshl_b32 s31, s2, 8
	s_lshl_b32 s33, s3, 10
	s_lshl_b32 s34, s3, 8
	s_addk_i32 s34, 0x4000
	s_waitcnt lgkmcnt(0)
	s_add_u32 s6, s6, s30
	s_addc_u32 s7, s7, 0
	s_add_u32 s8, s8, s30
	s_addc_u32 s9, s9, 0
	s_load_dword s35, s[6:7], 0x0
	s_load_dword s36, s[8:9], 0x0
	s_add_u32 s10, s10, s28
	s_addc_u32 s11, s11, 0
	s_add_u32 s18, s18, s33
	s_addc_u32 s19, s19, 0
	s_add_u32 s14, s14, s29
	s_addc_u32 s15, s15, 0
	s_add_u32 s12, s12, s31
	s_addc_u32 s13, s13, 0
	s_add_u32 s16, s16, s31
	s_addc_u32 s17, s17, 0
	s_waitcnt lgkmcnt(0)
	s_lshl_b32 s36, s36, 7
	s_add_u32 s20, s20, s36
	s_addc_u32 s21, s21, 0
	s_lshl_b32 s37, s35, 7
	s_add_u32 s4, s4, s37
	s_addc_u32 s5, s5, 0
	global_load_dwordx4 v[64:67], v78, s[4:5] nt
	global_load_dwordx4 v[68:71], v78, s[4:5] offset:16 nt
	v_add_u32_e32 v78, s34, v77
	s_waitcnt vmcnt(0)
	v_cvt_f32_f16_e32 v80, v64
	v_cvt_f32_f16_sdwa v81, v64 dst_sel:DWORD dst_unused:UNUSED_PAD src0_sel:WORD_1
	v_cvt_f32_f16_e32 v82, v65
	v_cvt_f32_f16_sdwa v83, v65 dst_sel:DWORD dst_unused:UNUSED_PAD src0_sel:WORD_1
	v_cvt_f32_f16_e32 v84, v66
	v_cvt_f32_f16_sdwa v85, v66 dst_sel:DWORD dst_unused:UNUSED_PAD src0_sel:WORD_1
	v_cvt_f32_f16_e32 v86, v67
	v_cvt_f32_f16_sdwa v87, v67 dst_sel:DWORD dst_unused:UNUSED_PAD src0_sel:WORD_1
	v_cvt_f32_f16_e32 v88, v68
	v_cvt_f32_f16_sdwa v89, v68 dst_sel:DWORD dst_unused:UNUSED_PAD src0_sel:WORD_1
	v_cvt_f32_f16_e32 v90, v69
	v_cvt_f32_f16_sdwa v91, v69 dst_sel:DWORD dst_unused:UNUSED_PAD src0_sel:WORD_1
	v_cvt_f32_f16_e32 v92, v70
	v_cvt_f32_f16_sdwa v93, v70 dst_sel:DWORD dst_unused:UNUSED_PAD src0_sel:WORD_1
	v_cvt_f32_f16_e32 v94, v71
	v_cvt_f32_f16_sdwa v95, v71 dst_sel:DWORD dst_unused:UNUSED_PAD src0_sel:WORD_1
	v_max_f32_e32 v80, 0, v80
	v_max_f32_e32 v81, 0, v81
	v_max_f32_e32 v82, 0, v82
	v_max_f32_e32 v83, 0, v83
	v_max_f32_e32 v84, 0, v84
	v_max_f32_e32 v85, 0, v85
	v_max_f32_e32 v86, 0, v86
	v_max_f32_e32 v87, 0, v87
	v_max_f32_e32 v88, 0, v88
	v_max_f32_e32 v89, 0, v89
	v_max_f32_e32 v90, 0, v90
	v_max_f32_e32 v91, 0, v91
	v_max_f32_e32 v92, 0, v92
	v_max_f32_e32 v93, 0, v93
	v_max_f32_e32 v94, 0, v94
	v_max_f32_e32 v95, 0, v95
	v_cmp_neq_f32_e64 s[40:41], 0, v80
	v_cmp_neq_f32_e64 s[42:43], 0, v81
	v_cmp_neq_f32_e64 s[44:45], 0, v82
	v_cmp_neq_f32_e64 s[46:47], 0, v83
	v_cmp_neq_f32_e64 s[48:49], 0, v84
	v_cmp_neq_f32_e64 s[50:51], 0, v85
	v_cmp_neq_f32_e64 s[52:53], 0, v86
	v_cmp_neq_f32_e64 s[54:55], 0, v87
	v_cmp_neq_f32_e64 s[56:57], 0, v88
	v_cmp_neq_f32_e64 s[58:59], 0, v89
	v_cmp_neq_f32_e64 s[60:61], 0, v90
	v_cmp_neq_f32_e64 s[62:63], 0, v91
	v_cmp_neq_f32_e64 s[64:65], 0, v92
	v_cmp_neq_f32_e64 s[66:67], 0, v93
	v_cmp_neq_f32_e64 s[68:69], 0, v94
	v_cmp_neq_f32_e64 s[70:71], 0, v95
	v_lshlrev_b32_e32 v96, 12, v75
	v_lshl_or_b32 v96, v76, 4, v96
	s_mov_b64 exec, s[40:41]
	global_load_dwordx4 v[0:3], v96, s[10:11] nt
	s_mov_b64 exec, s[42:43]
	global_load_dwordx4 v[4:7], v96, s[10:11] offset:256 nt
	s_mov_b64 exec, s[44:45]
	global_load_dwordx4 v[8:11], v96, s[10:11] offset:512 nt
	s_mov_b64 exec, s[46:47]
	global_load_dwordx4 v[12:15], v96, s[10:11] offset:768 nt
	s_mov_b64 exec, s[48:49]
	global_load_dwordx4 v[16:19], v96, s[10:11] offset:1024 nt
	s_mov_b64 exec, s[50:51]
	global_load_dwordx4 v[20:23], v96, s[10:11] offset:1280 nt
	s_mov_b64 exec, s[52:53]
	global_load_dwordx4 v[24:27], v96, s[10:11] offset:1536 nt
	s_mov_b64 exec, s[54:55]
	global_load_dwordx4 v[28:31], v96, s[10:11] offset:1792 nt
	s_mov_b64 exec, s[56:57]
	global_load_dwordx4 v[32:35], v96, s[10:11] offset:2048 nt
	s_mov_b64 exec, s[58:59]
	global_load_dwordx4 v[36:39], v96, s[10:11] offset:2304 nt
	s_mov_b64 exec, s[60:61]
	global_load_dwordx4 v[40:43], v96, s[10:11] offset:2560 nt
	s_mov_b64 exec, s[62:63]
	global_load_dwordx4 v[44:47], v96, s[10:11] offset:2816 nt
	s_mov_b64 exec, s[64:65]
	global_load_dwordx4 v[48:51], v96, s[10:11] offset:3072 nt
	s_mov_b64 exec, s[66:67]
	global_load_dwordx4 v[52:55], v96, s[10:11] offset:3328 nt
	s_mov_b64 exec, s[68:69]
	global_load_dwordx4 v[56:59], v96, s[10:11] offset:3584 nt
	s_mov_b64 exec, s[70:71]
	global_load_dwordx4 v[60:63], v96, s[10:11] offset:3840 nt
	s_mov_b64 exec, -1
	s_mov_b32 m0, s33
	s_nop 0
	global_load_lds_dwordx4 v79, s[18:19]
	global_load_lds_dwordx4 v79, s[18:19] offset:2048
	s_add_u32 m0, m0, 0x1000
	s_add_u32 s18, s18, 0x1000
	s_addc_u32 s19, s19, 0
	global_load_lds_dwordx4 v79, s[18:19]
	global_load_lds_dwordx4 v79, s[18:19] offset:2048
	s_add_u32 m0, m0, 0x1000
	s_add_u32 s18, s18, 0x1000
	s_addc_u32 s19, s19, 0
	global_load_lds_dwordx4 v79, s[18:19]
	global_load_lds_dwordx4 v79, s[18:19] offset:2048
	s_add_u32 m0, m0, 0x1000
	s_add_u32 s18, s18, 0x1000
	s_addc_u32 s19, s19, 0
	global_load_lds_dwordx4 v79, s[18:19]
	global_load_lds_dwordx4 v79, s[18:19] offset:2048
	global_load_dword v72, v77, s[12:13] nt
	global_load_dword v73, v77, s[16:17] nt
	v_lshl_add_u32 v79, v75, 2, s34
	v_mov_b32_e32 v96, 0
	v_mov_b32_e32 v97, 0
	v_mov_b32_e32 v98, 0
	v_mov_b32_e32 v99, 0
	v_mov_b32_e32 v100, 0
	v_mov_b32_e32 v101, 0
	v_mov_b32_e32 v102, 0
	v_mov_b32_e32 v103, 0
	s_waitcnt vmcnt(0)
	s_barrier
	s_setprio 3
	s_mov_b64 exec, s[40:41]
	v_pk_fma_f32 v[96:97], v[80:81], v[0:1], v[96:97] op_sel_hi:[0,1,1]
	v_pk_fma_f32 v[98:99], v[80:81], v[2:3], v[98:99] op_sel_hi:[0,1,1]
	s_mov_b64 exec, s[42:43]
	v_pk_fma_f32 v[100:101], v[80:81], v[4:5], v[100:101] op_sel:[1,0,0]
	v_pk_fma_f32 v[102:103], v[80:81], v[6:7], v[102:103] op_sel:[1,0,0]
	s_mov_b64 exec, s[44:45]
	v_pk_fma_f32 v[96:97], v[82:83], v[8:9], v[96:97] op_sel_hi:[0,1,1]
	v_pk_fma_f32 v[98:99], v[82:83], v[10:11], v[98:99] op_sel_hi:[0,1,1]
	s_mov_b64 exec, s[46:47]
	v_pk_fma_f32 v[100:101], v[82:83], v[12:13], v[100:101] op_sel:[1,0,0]
	v_pk_fma_f32 v[102:103], v[82:83], v[14:15], v[102:103] op_sel:[1,0,0]
	s_mov_b64 exec, s[48:49]
	v_pk_fma_f32 v[96:97], v[84:85], v[16:17], v[96:97] op_sel_hi:[0,1,1]
	v_pk_fma_f32 v[98:99], v[84:85], v[18:19], v[98:99] op_sel_hi:[0,1,1]
	s_mov_b64 exec, s[50:51]
	v_pk_fma_f32 v[100:101], v[84:85], v[20:21], v[100:101] op_sel:[1,0,0]
	v_pk_fma_f32 v[102:103], v[84:85], v[22:23], v[102:103] op_sel:[1,0,0]
	s_mov_b64 exec, s[52:53]
	v_pk_fma_f32 v[96:97], v[86:87], v[24:25], v[96:97] op_sel_hi:[0,1,1]
	v_pk_fma_f32 v[98:99], v[86:87], v[26:27], v[98:99] op_sel_hi:[0,1,1]
	s_mov_b64 exec, s[54:55]
	v_pk_fma_f32 v[100:101], v[86:87], v[28:29], v[100:101] op_sel:[1,0,0]
	v_pk_fma_f32 v[102:103], v[86:87], v[30:31], v[102:103] op_sel:[1,0,0]
	s_mov_b64 exec, s[56:57]
	v_pk_fma_f32 v[96:97], v[88:89], v[32:33], v[96:97] op_sel_hi:[0,1,1]
	v_pk_fma_f32 v[98:99], v[88:89], v[34:35], v[98:99] op_sel_hi:[0,1,1]
	s_mov_b64 exec, s[58:59]
	v_pk_fma_f32 v[100:101], v[88:89], v[36:37], v[100:101] op_sel:[1,0,0]
	v_pk_fma_f32 v[102:103], v[88:89], v[38:39], v[102:103] op_sel:[1,0,0]
	s_mov_b64 exec, s[60:61]
	v_pk_fma_f32 v[96:97], v[90:91], v[40:41], v[96:97] op_sel_hi:[0,1,1]
	v_pk_fma_f32 v[98:99], v[90:91], v[42:43], v[98:99] op_sel_hi:[0,1,1]
	s_mov_b64 exec, s[62:63]
	v_pk_fma_f32 v[100:101], v[90:91], v[44:45], v[100:101] op_sel:[1,0,0]
	v_pk_fma_f32 v[102:103], v[90:91], v[46:47], v[102:103] op_sel:[1,0,0]
	s_mov_b64 exec, s[64:65]
	v_pk_fma_f32 v[96:97], v[92:93], v[48:49], v[96:97] op_sel_hi:[0,1,1]
	v_pk_fma_f32 v[98:99], v[92:93], v[50:51], v[98:99] op_sel_hi:[0,1,1]
	s_mov_b64 exec, s[66:67]
	v_pk_fma_f32 v[100:101], v[92:93], v[52:53], v[100:101] op_sel:[1,0,0]
	v_pk_fma_f32 v[102:103], v[92:93], v[54:55], v[102:103] op_sel:[1,0,0]
	s_mov_b64 exec, s[68:69]
	v_pk_fma_f32 v[96:97], v[94:95], v[56:57], v[96:97] op_sel_hi:[0,1,1]
	v_pk_fma_f32 v[98:99], v[94:95], v[58:59], v[98:99] op_sel_hi:[0,1,1]
	s_mov_b64 exec, s[70:71]
	v_pk_fma_f32 v[100:101], v[94:95], v[60:61], v[100:101] op_sel:[1,0,0]
	v_pk_fma_f32 v[102:103], v[94:95], v[62:63], v[102:103] op_sel:[1,0,0]
	s_mov_b64 exec, -1
	v_pk_add_f32 v[96:97], v[96:97], v[100:101]
	v_pk_add_f32 v[98:99], v[98:99], v[102:103]
	s_nop 1
	v_permlane16_swap_b32_e32 v96, v97
	v_permlane16_swap_b32_e32 v98, v99
	v_add_f32_e32 v96, v96, v97
	v_add_f32_e32 v98, v98, v99
	s_nop 1
	v_permlane32_swap_b32_e32 v96, v98
	v_add_f32_e32 v96, v96, v98
	s_waitcnt vmcnt(1)
	v_add_f32_e32 v96, v96, v72
	v_max_f32_e32 v96, 0, v96
	ds_write_b32 v78, v96
	ds_read2_b32 v[80:81], v79 offset0:0 offset1:4
	ds_read2_b32 v[82:83], v79 offset0:8 offset1:12
	ds_read2_b32 v[84:85], v79 offset0:16 offset1:20
	ds_read2_b32 v[86:87], v79 offset0:24 offset1:28
	ds_read2_b32 v[88:89], v79 offset0:32 offset1:36
	ds_read2_b32 v[90:91], v79 offset0:40 offset1:44
	ds_read2_b32 v[92:93], v79 offset0:48 offset1:52
	ds_read2_b32 v[94:95], v79 offset0:56 offset1:60
	s_waitcnt lgkmcnt(0)
	v_cmp_neq_f32_e64 s[40:41], 0, v80
	v_cmp_neq_f32_e64 s[42:43], 0, v81
	v_cmp_neq_f32_e64 s[44:45], 0, v82
	v_cmp_neq_f32_e64 s[46:47], 0, v83
	v_cmp_neq_f32_e64 s[48:49], 0, v84
	v_cmp_neq_f32_e64 s[50:51], 0, v85
	v_cmp_neq_f32_e64 s[52:53], 0, v86
	v_cmp_neq_f32_e64 s[54:55], 0, v87
	v_cmp_neq_f32_e64 s[56:57], 0, v88
	v_cmp_neq_f32_e64 s[58:59], 0, v89
	v_cmp_neq_f32_e64 s[60:61], 0, v90
	v_cmp_neq_f32_e64 s[62:63], 0, v91
	v_cmp_neq_f32_e64 s[64:65], 0, v92
	v_cmp_neq_f32_e64 s[66:67], 0, v93
	v_cmp_neq_f32_e64 s[68:69], 0, v94
	v_cmp_neq_f32_e64 s[70:71], 0, v95
	s_mov_b64 exec, s[40:41]
	global_load_dwordx4 v[0:3], v74, s[14:15] nt
	s_mov_b64 exec, s[42:43]
	global_load_dwordx4 v[4:7], v74, s[14:15] offset:1024 nt
	s_mov_b64 exec, s[44:45]
	global_load_dwordx4 v[8:11], v74, s[14:15] offset:2048 nt
	s_mov_b64 exec, s[46:47]
	global_load_dwordx4 v[12:15], v74, s[14:15] offset:3072 nt
	s_add_u32 s14, s14, 0x1000
	s_addc_u32 s15, s15, 0
	s_mov_b64 exec, s[48:49]
	global_load_dwordx4 v[16:19], v74, s[14:15] nt
	s_mov_b64 exec, s[50:51]
	global_load_dwordx4 v[20:23], v74, s[14:15] offset:1024 nt
	s_mov_b64 exec, s[52:53]
	global_load_dwordx4 v[24:27], v74, s[14:15] offset:2048 nt
	s_mov_b64 exec, s[54:55]
	global_load_dwordx4 v[28:31], v74, s[14:15] offset:3072 nt
	s_add_u32 s14, s14, 0x1000
	s_addc_u32 s15, s15, 0
	s_mov_b64 exec, s[56:57]
	global_load_dwordx4 v[32:35], v74, s[14:15] nt
	s_mov_b64 exec, s[58:59]
	global_load_dwordx4 v[36:39], v74, s[14:15] offset:1024 nt
	s_mov_b64 exec, s[60:61]
	global_load_dwordx4 v[40:43], v74, s[14:15] offset:2048 nt
	s_mov_b64 exec, s[62:63]
	global_load_dwordx4 v[44:47], v74, s[14:15] offset:3072 nt
	s_add_u32 s14, s14, 0x1000
	s_addc_u32 s15, s15, 0
	s_mov_b64 exec, s[64:65]
	global_load_dwordx4 v[48:51], v74, s[14:15] nt
	s_mov_b64 exec, s[66:67]
	global_load_dwordx4 v[52:55], v74, s[14:15] offset:1024 nt
	s_mov_b64 exec, s[68:69]
	global_load_dwordx4 v[56:59], v74, s[14:15] offset:2048 nt
	s_mov_b64 exec, s[70:71]
	global_load_dwordx4 v[60:63], v74, s[14:15] offset:3072 nt
	s_mov_b64 exec, -1
	v_mov_b32_e32 v96, 0
	v_mov_b32_e32 v97, 0
	v_mov_b32_e32 v98, 0
	v_mov_b32_e32 v99, 0
	v_mov_b32_e32 v100, 0
	v_mov_b32_e32 v101, 0
	v_mov_b32_e32 v102, 0
	v_mov_b32_e32 v103, 0
	s_waitcnt vmcnt(0)
	s_mov_b64 exec, s[40:41]
	v_pk_fma_f32 v[96:97], v[80:81], v[0:1], v[96:97] op_sel_hi:[0,1,1]
	v_pk_fma_f32 v[98:99], v[80:81], v[2:3], v[98:99] op_sel_hi:[0,1,1]
	s_mov_b64 exec, s[42:43]
	v_pk_fma_f32 v[100:101], v[80:81], v[4:5], v[100:101] op_sel:[1,0,0]
	v_pk_fma_f32 v[102:103], v[80:81], v[6:7], v[102:103] op_sel:[1,0,0]
	s_mov_b64 exec, s[44:45]
	v_pk_fma_f32 v[96:97], v[82:83], v[8:9], v[96:97] op_sel_hi:[0,1,1]
	v_pk_fma_f32 v[98:99], v[82:83], v[10:11], v[98:99] op_sel_hi:[0,1,1]
	s_mov_b64 exec, s[46:47]
	v_pk_fma_f32 v[100:101], v[82:83], v[12:13], v[100:101] op_sel:[1,0,0]
	v_pk_fma_f32 v[102:103], v[82:83], v[14:15], v[102:103] op_sel:[1,0,0]
	s_mov_b64 exec, s[48:49]
	v_pk_fma_f32 v[96:97], v[84:85], v[16:17], v[96:97] op_sel_hi:[0,1,1]
	v_pk_fma_f32 v[98:99], v[84:85], v[18:19], v[98:99] op_sel_hi:[0,1,1]
	s_mov_b64 exec, s[50:51]
	v_pk_fma_f32 v[100:101], v[84:85], v[20:21], v[100:101] op_sel:[1,0,0]
	v_pk_fma_f32 v[102:103], v[84:85], v[22:23], v[102:103] op_sel:[1,0,0]
	s_mov_b64 exec, s[52:53]
	v_pk_fma_f32 v[96:97], v[86:87], v[24:25], v[96:97] op_sel_hi:[0,1,1]
	v_pk_fma_f32 v[98:99], v[86:87], v[26:27], v[98:99] op_sel_hi:[0,1,1]
	s_mov_b64 exec, s[54:55]
	v_pk_fma_f32 v[100:101], v[86:87], v[28:29], v[100:101] op_sel:[1,0,0]
	v_pk_fma_f32 v[102:103], v[86:87], v[30:31], v[102:103] op_sel:[1,0,0]
	s_mov_b64 exec, s[56:57]
	v_pk_fma_f32 v[96:97], v[88:89], v[32:33], v[96:97] op_sel_hi:[0,1,1]
	v_pk_fma_f32 v[98:99], v[88:89], v[34:35], v[98:99] op_sel_hi:[0,1,1]
	s_mov_b64 exec, s[58:59]
	v_pk_fma_f32 v[100:101], v[88:89], v[36:37], v[100:101] op_sel:[1,0,0]
	v_pk_fma_f32 v[102:103], v[88:89], v[38:39], v[102:103] op_sel:[1,0,0]
	s_mov_b64 exec, s[60:61]
	v_pk_fma_f32 v[96:97], v[90:91], v[40:41], v[96:97] op_sel_hi:[0,1,1]
	v_pk_fma_f32 v[98:99], v[90:91], v[42:43], v[98:99] op_sel_hi:[0,1,1]
	s_mov_b64 exec, s[62:63]
	v_pk_fma_f32 v[100:101], v[90:91], v[44:45], v[100:101] op_sel:[1,0,0]
	v_pk_fma_f32 v[102:103], v[90:91], v[46:47], v[102:103] op_sel:[1,0,0]
	s_mov_b64 exec, s[64:65]
	v_pk_fma_f32 v[96:97], v[92:93], v[48:49], v[96:97] op_sel_hi:[0,1,1]
	v_pk_fma_f32 v[98:99], v[92:93], v[50:51], v[98:99] op_sel_hi:[0,1,1]
	s_mov_b64 exec, s[66:67]
	v_pk_fma_f32 v[100:101], v[92:93], v[52:53], v[100:101] op_sel:[1,0,0]
	v_pk_fma_f32 v[102:103], v[92:93], v[54:55], v[102:103] op_sel:[1,0,0]
	s_mov_b64 exec, s[68:69]
	v_pk_fma_f32 v[96:97], v[94:95], v[56:57], v[96:97] op_sel_hi:[0,1,1]
	v_pk_fma_f32 v[98:99], v[94:95], v[58:59], v[98:99] op_sel_hi:[0,1,1]
	s_mov_b64 exec, s[70:71]
	v_pk_fma_f32 v[100:101], v[94:95], v[60:61], v[100:101] op_sel:[1,0,0]
	v_pk_fma_f32 v[102:103], v[94:95], v[62:63], v[102:103] op_sel:[1,0,0]
	s_mov_b64 exec, -1
	ds_read_b128 v[0:3], v74
	ds_read_b128 v[4:7], v74 offset:1024
	ds_read_b128 v[8:11], v74 offset:2048
	ds_read_b128 v[12:15], v74 offset:3072
	ds_read_b128 v[16:19], v74 offset:4096
	ds_read_b128 v[20:23], v74 offset:5120
	ds_read_b128 v[24:27], v74 offset:6144
	ds_read_b128 v[28:31], v74 offset:7168
	ds_read_b128 v[32:35], v74 offset:8192
	ds_read_b128 v[36:39], v74 offset:9216
	ds_read_b128 v[40:43], v74 offset:10240
	ds_read_b128 v[44:47], v74 offset:11264
	ds_read_b128 v[48:51], v74 offset:12288
	ds_read_b128 v[52:55], v74 offset:13312
	ds_read_b128 v[56:59], v74 offset:14336
	v_pk_add_f32 v[96:97], v[96:97], v[100:101]
	v_pk_add_f32 v[98:99], v[98:99], v[102:103]
	s_nop 1
	v_permlane16_swap_b32_e32 v96, v97
	v_permlane16_swap_b32_e32 v98, v99
	v_add_f32_e32 v96, v96, v97
	v_add_f32_e32 v98, v98, v99
	s_nop 1
	v_permlane32_swap_b32_e32 v96, v98
	v_add_f32_e32 v96, v96, v98
	v_add_f32_e32 v96, v96, v73
	s_waitcnt lgkmcnt(5)
	ds_read_b128 v[60:63], v74 offset:15360
	ds_write_b32 v78, v96
	ds_read2_b32 v[80:81], v79 offset0:0 offset1:4
	ds_read2_b32 v[82:83], v79 offset0:8 offset1:12
	ds_read2_b32 v[84:85], v79 offset0:16 offset1:20
	ds_read2_b32 v[86:87], v79 offset0:24 offset1:28
	ds_read2_b32 v[88:89], v79 offset0:32 offset1:36
	ds_read2_b32 v[90:91], v79 offset0:40 offset1:44
	ds_read2_b32 v[92:93], v79 offset0:48 offset1:52
	ds_read2_b32 v[94:95], v79 offset0:56 offset1:60
	v_lshlrev_b32_e32 v72, 3, v76
	v_lshl_or_b32 v72, v75, 2, v72
	v_cmp_gt_u32_e32 vcc, 2, v75
	s_waitcnt lgkmcnt(0)
	v_pk_mul_f32 v[96:97], v[80:81], v[0:1] op_sel_hi:[0,1]
	v_pk_mul_f32 v[98:99], v[80:81], v[2:3] op_sel_hi:[0,1]
	v_pk_mul_f32 v[100:101], v[80:81], v[4:5] op_sel:[1,0]
	v_pk_mul_f32 v[102:103], v[80:81], v[6:7] op_sel:[1,0]
	v_pk_fma_f32 v[96:97], v[82:83], v[8:9], v[96:97] op_sel_hi:[0,1,1]
	v_pk_fma_f32 v[98:99], v[82:83], v[10:11], v[98:99] op_sel_hi:[0,1,1]
	v_pk_fma_f32 v[100:101], v[82:83], v[12:13], v[100:101] op_sel:[1,0,0]
	v_pk_fma_f32 v[102:103], v[82:83], v[14:15], v[102:103] op_sel:[1,0,0]
	v_pk_fma_f32 v[96:97], v[84:85], v[16:17], v[96:97] op_sel_hi:[0,1,1]
	v_pk_fma_f32 v[98:99], v[84:85], v[18:19], v[98:99] op_sel_hi:[0,1,1]
	v_pk_fma_f32 v[100:101], v[84:85], v[20:21], v[100:101] op_sel:[1,0,0]
	v_pk_fma_f32 v[102:103], v[84:85], v[22:23], v[102:103] op_sel:[1,0,0]
	v_pk_fma_f32 v[96:97], v[86:87], v[24:25], v[96:97] op_sel_hi:[0,1,1]
	v_pk_fma_f32 v[98:99], v[86:87], v[26:27], v[98:99] op_sel_hi:[0,1,1]
	v_pk_fma_f32 v[100:101], v[86:87], v[28:29], v[100:101] op_sel:[1,0,0]
	v_pk_fma_f32 v[102:103], v[86:87], v[30:31], v[102:103] op_sel:[1,0,0]
	v_pk_fma_f32 v[96:97], v[88:89], v[32:33], v[96:97] op_sel_hi:[0,1,1]
	v_pk_fma_f32 v[98:99], v[88:89], v[34:35], v[98:99] op_sel_hi:[0,1,1]
	v_pk_fma_f32 v[100:101], v[88:89], v[36:37], v[100:101] op_sel:[1,0,0]
	v_pk_fma_f32 v[102:103], v[88:89], v[38:39], v[102:103] op_sel:[1,0,0]
	v_pk_fma_f32 v[96:97], v[90:91], v[40:41], v[96:97] op_sel_hi:[0,1,1]
	v_pk_fma_f32 v[98:99], v[90:91], v[42:43], v[98:99] op_sel_hi:[0,1,1]
	v_pk_fma_f32 v[100:101], v[90:91], v[44:45], v[100:101] op_sel:[1,0,0]
	v_pk_fma_f32 v[102:103], v[90:91], v[46:47], v[102:103] op_sel:[1,0,0]
	v_pk_fma_f32 v[96:97], v[92:93], v[48:49], v[96:97] op_sel_hi:[0,1,1]
	v_pk_fma_f32 v[98:99], v[92:93], v[50:51], v[98:99] op_sel_hi:[0,1,1]
	v_pk_fma_f32 v[100:101], v[92:93], v[52:53], v[100:101] op_sel:[1,0,0]
	v_pk_fma_f32 v[102:103], v[92:93], v[54:55], v[102:103] op_sel:[1,0,0]
	v_pk_fma_f32 v[96:97], v[94:95], v[56:57], v[96:97] op_sel_hi:[0,1,1]
	v_pk_fma_f32 v[98:99], v[94:95], v[58:59], v[98:99] op_sel_hi:[0,1,1]
	v_pk_fma_f32 v[100:101], v[94:95], v[60:61], v[100:101] op_sel:[1,0,0]
	v_pk_fma_f32 v[102:103], v[94:95], v[62:63], v[102:103] op_sel:[1,0,0]
	v_pk_add_f32 v[96:97], v[96:97], v[100:101]
	v_pk_add_f32 v[98:99], v[98:99], v[102:103]
	s_nop 1
	v_permlane16_swap_b32_e32 v96, v98
	v_permlane16_swap_b32_e32 v97, v99
	v_add_f32_e32 v96, v96, v98
	v_add_f32_e32 v97, v97, v99
	v_mov_b32_e32 v80, v96
	v_mov_b32_e32 v81, v97
	s_nop 1
	v_permlane32_swap_b32_e32 v96, v80
	v_permlane32_swap_b32_e32 v97, v81
	v_add_f32_e32 v96, v96, v80
	v_add_f32_e32 v97, v97, v81
	v_cvt_pk_f16_f32 v73, v96, v97
	s_and_saveexec_b64 s[4:5], vcc
	global_atomic_pk_add_f16 v72, v73, s[20:21]
	s_endpgm
	.p2align	8
